# proj/MLP2: first-iteration-only load blocks moved out of line so the steady-state path has no taken branch
# baseline (speedup 1.0000x reference)
.LBB4_22:
	s_mov_b32 m0, s70
	ds_read_b128 v[130:133], v136 offset:16384
	ds_read_b128 v[142:145], v136 offset:17408
	ds_read_b128 v[146:149], v136 offset:18432
	ds_read_b128 v[150:153], v136 offset:19456
	ds_read_b128 v[154:157], v137
	ds_read_b128 v[158:161], v137 offset:1024
	ds_read_b128 v[162:165], v137 offset:2048
	ds_read_b128 v[166:169], v137 offset:3072
	ds_read_b128 v[170:173], v137 offset:4096
	ds_read_b128 v[174:177], v137 offset:5120
	ds_read_b128 v[178:181], v137 offset:6144
	ds_read_b128 v[182:185], v137 offset:7168
	global_load_lds_dwordx4 v0, s[74:75]
	s_add_i32 m0, s70, 0x2000
	s_nop 0
	global_load_lds_dwordx4 v120, s[74:75]
	s_barrier
	s_setprio 1
	s_waitcnt lgkmcnt(7)
	v_mfma_f32_16x16x32_f16 v[94:97], v[130:133], v[154:157], v[94:97]
	v_mfma_f32_16x16x32_f16 v[90:93], v[146:149], v[154:157], v[90:93]
	s_waitcnt lgkmcnt(5)
	v_mfma_f32_16x16x32_f16 v[82:85], v[130:133], v[162:165], v[82:85]
	v_mfma_f32_16x16x32_f16 v[78:81], v[146:149], v[162:165], v[78:81]
	s_waitcnt lgkmcnt(3)
	v_mfma_f32_16x16x32_f16 v[70:73], v[130:133], v[170:173], v[70:73]
	v_mfma_f32_16x16x32_f16 v[66:69], v[146:149], v[170:173], v[66:69]
	s_waitcnt lgkmcnt(1)
	v_mfma_f32_16x16x32_f16 v[58:61], v[130:133], v[178:181], v[58:61]
	v_mfma_f32_16x16x32_f16 v[54:57], v[146:149], v[178:181], v[54:57]
	v_mfma_f32_16x16x32_f16 v[94:97], v[142:145], v[158:161], v[94:97]
	v_mfma_f32_16x16x32_f16 v[90:93], v[150:153], v[158:161], v[90:93]
	v_mfma_f32_16x16x32_f16 v[82:85], v[142:145], v[166:169], v[82:85]
	v_mfma_f32_16x16x32_f16 v[78:81], v[150:153], v[166:169], v[78:81]
	v_mfma_f32_16x16x32_f16 v[70:73], v[142:145], v[174:177], v[70:73]
	v_mfma_f32_16x16x32_f16 v[66:69], v[150:153], v[174:177], v[66:69]
	s_waitcnt lgkmcnt(0)
	v_mfma_f32_16x16x32_f16 v[58:61], v[142:145], v[182:185], v[58:61]
	v_mfma_f32_16x16x32_f16 v[54:57], v[150:153], v[182:185], v[54:57]
	s_setprio 0
	s_barrier
	s_add_i32 m0, s49, 0x18000
	ds_read_b128 v[130:133], v136 offset:20480
	ds_read_b128 v[142:145], v136 offset:21504
	global_load_lds_dwordx4 v122, s[76:77]
	s_add_i32 m0, s49, 0x1a000
	s_nop 0
	global_load_lds_dwordx4 v124, s[76:77]
	s_add_i32 m0, s49, 0x1c000
	s_nop 0
	global_load_lds_dwordx4 v126, s[76:77]
	s_cmp_eq_u32 s67, 0
	s_cbranch_scc1 .Lpj_first_0
	s_waitcnt vmcnt(5)
.Lpj_join_0:
	s_barrier
	s_setprio 1
	s_waitcnt lgkmcnt(1)
	v_mfma_f32_16x16x32_f16 v[86:89], v[130:133], v[154:157], v[86:89]
	v_mfma_f32_16x16x32_f16 v[74:77], v[130:133], v[162:165], v[74:77]
	v_mfma_f32_16x16x32_f16 v[62:65], v[130:133], v[170:173], v[62:65]
	v_mfma_f32_16x16x32_f16 v[50:53], v[130:133], v[178:181], v[50:53]
	s_waitcnt lgkmcnt(0)
	v_mfma_f32_16x16x32_f16 v[86:89], v[142:145], v[158:161], v[86:89]
	v_mfma_f32_16x16x32_f16 v[74:77], v[142:145], v[166:169], v[74:77]
	v_mfma_f32_16x16x32_f16 v[62:65], v[142:145], v[174:177], v[62:65]
	v_mfma_f32_16x16x32_f16 v[50:53], v[142:145], v[182:185], v[50:53]
	s_setprio 0
	s_barrier
	s_mov_b32 m0, s49
	ds_read_b128 v[130:133], v136 offset:57344
	ds_read_b128 v[142:145], v136 offset:58368
	ds_read_b128 v[146:149], v136 offset:59392
	ds_read_b128 v[150:153], v136 offset:60416
	ds_read_b128 v[154:157], v137 offset:40960
	ds_read_b128 v[158:161], v137 offset:41984
	ds_read_b128 v[162:165], v137 offset:43008
	ds_read_b128 v[166:169], v137 offset:44032
	ds_read_b128 v[170:173], v137 offset:45056
	ds_read_b128 v[174:177], v137 offset:46080
	ds_read_b128 v[178:181], v137 offset:47104
	ds_read_b128 v[182:185], v137 offset:48128
	global_load_lds_dwordx4 v110, s[68:69]
	s_mov_b32 m0, s50
	s_nop 0
	global_load_lds_dwordx4 v114, s[68:69]
	s_barrier
	s_setprio 1
	s_waitcnt lgkmcnt(7)
	v_mfma_f32_16x16x32_f16 v[94:97], v[130:133], v[154:157], v[94:97]
	v_mfma_f32_16x16x32_f16 v[90:93], v[146:149], v[154:157], v[90:93]
	s_waitcnt lgkmcnt(5)
	v_mfma_f32_16x16x32_f16 v[82:85], v[130:133], v[162:165], v[82:85]
	v_mfma_f32_16x16x32_f16 v[78:81], v[146:149], v[162:165], v[78:81]
	s_waitcnt lgkmcnt(3)
	v_mfma_f32_16x16x32_f16 v[70:73], v[130:133], v[170:173], v[70:73]
	v_mfma_f32_16x16x32_f16 v[66:69], v[146:149], v[170:173], v[66:69]
	s_waitcnt lgkmcnt(1)
	v_mfma_f32_16x16x32_f16 v[58:61], v[130:133], v[178:181], v[58:61]
	v_mfma_f32_16x16x32_f16 v[54:57], v[146:149], v[178:181], v[54:57]
	v_mfma_f32_16x16x32_f16 v[94:97], v[142:145], v[158:161], v[94:97]
	v_mfma_f32_16x16x32_f16 v[90:93], v[150:153], v[158:161], v[90:93]
	v_mfma_f32_16x16x32_f16 v[82:85], v[142:145], v[166:169], v[82:85]
	v_mfma_f32_16x16x32_f16 v[78:81], v[150:153], v[166:169], v[78:81]
	v_mfma_f32_16x16x32_f16 v[70:73], v[142:145], v[174:177], v[70:73]
	v_mfma_f32_16x16x32_f16 v[66:69], v[150:153], v[174:177], v[66:69]
	s_waitcnt lgkmcnt(0)
	v_mfma_f32_16x16x32_f16 v[58:61], v[142:145], v[182:185], v[58:61]
	v_mfma_f32_16x16x32_f16 v[54:57], v[150:153], v[182:185], v[54:57]
	s_setprio 0
	s_barrier
	s_mov_b32 m0, s51
	ds_read_b128 v[130:133], v136 offset:61440
	ds_read_b128 v[142:145], v136 offset:62464
	global_load_lds_dwordx4 v112, s[34:35]
	s_mov_b32 m0, s52
	s_nop 0
	global_load_lds_dwordx4 v116, s[34:35]
	s_mov_b32 m0, s53
	s_nop 0
	global_load_lds_dwordx4 v118, s[34:35]
	s_cmp_eq_u32 s67, 0
	s_cbranch_scc1 .Lpj_first_1
	s_waitcnt vmcnt(5)
.Lpj_join_1:
	s_barrier
	s_setprio 1
	s_waitcnt lgkmcnt(1)
	v_mfma_f32_16x16x32_f16 v[86:89], v[130:133], v[154:157], v[86:89]
	v_mfma_f32_16x16x32_f16 v[74:77], v[130:133], v[162:165], v[74:77]
	v_mfma_f32_16x16x32_f16 v[62:65], v[130:133], v[170:173], v[62:65]
	v_mfma_f32_16x16x32_f16 v[50:53], v[130:133], v[178:181], v[50:53]
	s_waitcnt lgkmcnt(0)
	v_mfma_f32_16x16x32_f16 v[86:89], v[142:145], v[158:161], v[86:89]
	v_mfma_f32_16x16x32_f16 v[74:77], v[142:145], v[166:169], v[74:77]
	v_mfma_f32_16x16x32_f16 v[62:65], v[142:145], v[174:177], v[62:65]
	v_mfma_f32_16x16x32_f16 v[50:53], v[142:145], v[182:185], v[50:53]
	s_setprio 0
	s_barrier
	s_mov_b32 m0, s56
	ds_read_b128 v[130:133], v138
	ds_read_b128 v[142:145], v138 offset:1024
	ds_read_b128 v[146:149], v138 offset:2048
	ds_read_b128 v[150:153], v138 offset:3072
	ds_read_b128 v[154:157], v139
	ds_read_b128 v[158:161], v139 offset:1024
	ds_read_b128 v[162:165], v139 offset:2048
	ds_read_b128 v[166:169], v139 offset:3072
	ds_read_b128 v[170:173], v139 offset:4096
	ds_read_b128 v[174:177], v139 offset:5120
	ds_read_b128 v[178:181], v139 offset:6144
	ds_read_b128 v[182:185], v139 offset:7168
	global_load_lds_dwordx4 v110, s[78:79]
	s_mov_b32 m0, s57
	s_nop 0
	global_load_lds_dwordx4 v114, s[78:79]
	s_barrier
	s_setprio 1
	s_waitcnt lgkmcnt(7)
	v_mfma_f32_16x16x32_f16 v[94:97], v[130:133], v[154:157], v[94:97]
	v_mfma_f32_16x16x32_f16 v[90:93], v[146:149], v[154:157], v[90:93]
	s_waitcnt lgkmcnt(5)
	v_mfma_f32_16x16x32_f16 v[82:85], v[130:133], v[162:165], v[82:85]
	v_mfma_f32_16x16x32_f16 v[78:81], v[146:149], v[162:165], v[78:81]
	s_waitcnt lgkmcnt(3)
	v_mfma_f32_16x16x32_f16 v[70:73], v[130:133], v[170:173], v[70:73]
	v_mfma_f32_16x16x32_f16 v[66:69], v[146:149], v[170:173], v[66:69]
	s_waitcnt lgkmcnt(1)
	v_mfma_f32_16x16x32_f16 v[58:61], v[130:133], v[178:181], v[58:61]
	v_mfma_f32_16x16x32_f16 v[54:57], v[146:149], v[178:181], v[54:57]
	v_mfma_f32_16x16x32_f16 v[94:97], v[142:145], v[158:161], v[94:97]
	v_mfma_f32_16x16x32_f16 v[90:93], v[150:153], v[158:161], v[90:93]
	v_mfma_f32_16x16x32_f16 v[82:85], v[142:145], v[166:169], v[82:85]
	v_mfma_f32_16x16x32_f16 v[78:81], v[150:153], v[166:169], v[78:81]
	v_mfma_f32_16x16x32_f16 v[70:73], v[142:145], v[174:177], v[70:73]
	v_mfma_f32_16x16x32_f16 v[66:69], v[150:153], v[174:177], v[66:69]
	s_waitcnt lgkmcnt(0)
	v_mfma_f32_16x16x32_f16 v[58:61], v[142:145], v[182:185], v[58:61]
	v_mfma_f32_16x16x32_f16 v[54:57], v[150:153], v[182:185], v[54:57]
	s_setprio 0
	s_barrier
	s_mov_b32 m0, s58
	ds_read_b128 v[130:133], v138 offset:4096
	ds_read_b128 v[142:145], v138 offset:5120
	global_load_lds_dwordx4 v112, s[80:81]
	s_add_i32 m0, s58, 0x2000
	s_nop 0
	global_load_lds_dwordx4 v116, s[80:81]
	s_add_i32 m0, s58, 0x4000
	s_nop 0
	global_load_lds_dwordx4 v118, s[80:81]
	s_cmp_eq_u32 s67, 0
	s_cbranch_scc1 .Lpj_first_2
	s_waitcnt vmcnt(5)

.Lpj_first_0:
	s_mul_i32 s72, s66, 0xc0
	v_add_u32_e32 v214, s72, v135
	v_ashrrev_i32_e32 v215, 31, v214
	v_lshl_add_u64 v[214:215], v[214:215], 2, s[10:11]
	global_load_dwordx4 v[202:205], v[214:215], off
	global_load_dwordx4 v[206:209], v[214:215], off offset:64
	global_load_dwordx4 v[210:213], v[214:215], off offset:128
	global_load_dwordx4 v[2:5], v[194:195], off
	global_load_dwordx4 v[6:9], v[194:195], off offset:64
	global_load_dwordx4 v[10:13], v[194:195], off offset:128
	global_load_dwordx4 v[14:17], v[196:197], off
	s_waitcnt vmcnt(12)
	s_branch .Lpj_join_0
.Lpj_first_1:
	global_load_dwordx4 v[18:21], v[196:197], off offset:64
	global_load_dwordx4 v[22:25], v[196:197], off offset:128
	global_load_dwordx4 v[26:29], v[198:199], off
	global_load_dwordx4 v[30:33], v[198:199], off offset:64
	s_waitcnt vmcnt(16)
	s_branch .Lpj_join_1
.Lpj_first_2:
	global_load_dwordx4 v[34:37], v[198:199], off offset:128
	global_load_dwordx4 v[38:41], v[200:201], off
	global_load_dwordx4 v[42:45], v[200:201], off offset:64
	global_load_dwordx4 v[46:49], v[200:201], off offset:128
	s_waitcnt vmcnt(13)
	s_branch .Lpj_join_2

.LBB6_22:
	s_mov_b32 m0, s68
	ds_read_b128 v[132:135], v131 offset:16384
	ds_read_b128 v[136:139], v131 offset:17408
	ds_read_b128 v[140:143], v131 offset:18432
	ds_read_b128 v[144:147], v131 offset:19456
	ds_read_b128 v[148:151], v182
	ds_read_b128 v[152:155], v182 offset:1024
	ds_read_b128 v[156:159], v182 offset:2048
	ds_read_b128 v[160:163], v182 offset:3072
	ds_read_b128 v[164:167], v182 offset:4096
	ds_read_b128 v[168:171], v182 offset:5120
	ds_read_b128 v[172:175], v182 offset:6144
	ds_read_b128 v[176:179], v182 offset:7168
	global_load_lds_dwordx4 v106, s[72:73]
	s_add_i32 m0, s68, 0x2000
	s_nop 0
	global_load_lds_dwordx4 v108, s[72:73]
	s_barrier
	s_setprio 1
	s_waitcnt lgkmcnt(7)
	v_mfma_f32_16x16x32_f16 v[40:43], v[132:135], v[148:151], v[40:43]
	v_mfma_f32_16x16x32_f16 v[44:47], v[140:143], v[148:151], v[44:47]
	s_waitcnt lgkmcnt(5)
	v_mfma_f32_16x16x32_f16 v[32:35], v[132:135], v[156:159], v[32:35]
	v_mfma_f32_16x16x32_f16 v[28:31], v[140:143], v[156:159], v[28:31]
	s_waitcnt lgkmcnt(3)
	v_mfma_f32_16x16x32_f16 v[20:23], v[132:135], v[164:167], v[20:23]
	v_mfma_f32_16x16x32_f16 v[16:19], v[140:143], v[164:167], v[16:19]
	s_waitcnt lgkmcnt(1)
	v_mfma_f32_16x16x32_f16 v[8:11], v[132:135], v[172:175], v[8:11]
	v_mfma_f32_16x16x32_f16 v[4:7], v[140:143], v[172:175], v[4:7]
	v_mfma_f32_16x16x32_f16 v[40:43], v[136:139], v[152:155], v[40:43]
	v_mfma_f32_16x16x32_f16 v[44:47], v[144:147], v[152:155], v[44:47]
	v_mfma_f32_16x16x32_f16 v[32:35], v[136:139], v[160:163], v[32:35]
	v_mfma_f32_16x16x32_f16 v[28:31], v[144:147], v[160:163], v[28:31]
	v_mfma_f32_16x16x32_f16 v[20:23], v[136:139], v[168:171], v[20:23]
	v_mfma_f32_16x16x32_f16 v[16:19], v[144:147], v[168:171], v[16:19]
	s_waitcnt lgkmcnt(0)
	v_mfma_f32_16x16x32_f16 v[8:11], v[136:139], v[176:179], v[8:11]
	v_mfma_f32_16x16x32_f16 v[4:7], v[144:147], v[176:179], v[4:7]
	s_setprio 0
	s_barrier
	s_add_i32 m0, s47, 0x18000
	ds_read_b128 v[132:135], v131 offset:20480
	ds_read_b128 v[136:139], v131 offset:21504
	global_load_lds_dwordx4 v110, s[74:75]
	s_add_i32 m0, s47, 0x1a000
	s_nop 0
	global_load_lds_dwordx4 v112, s[74:75]
	s_add_i32 m0, s47, 0x1c000
	s_nop 0
	global_load_lds_dwordx4 v114, s[74:75]
	s_cmp_eq_u32 s65, 0
	s_cbranch_scc1 .Lm2_first_0
	s_waitcnt vmcnt(5)
.Lm2_join_0:
	s_barrier
	s_setprio 1
	s_waitcnt lgkmcnt(1)
	v_mfma_f32_16x16x32_f16 v[36:39], v[132:135], v[148:151], v[36:39]
	v_mfma_f32_16x16x32_f16 v[24:27], v[132:135], v[156:159], v[24:27]
	v_mfma_f32_16x16x32_f16 v[12:15], v[132:135], v[164:167], v[12:15]
	v_mfma_f32_16x16x32_f16 v[0:3], v[132:135], v[172:175], v[0:3]
	s_waitcnt lgkmcnt(0)
	v_mfma_f32_16x16x32_f16 v[36:39], v[136:139], v[152:155], v[36:39]
	v_mfma_f32_16x16x32_f16 v[24:27], v[136:139], v[160:163], v[24:27]
	v_mfma_f32_16x16x32_f16 v[12:15], v[136:139], v[168:171], v[12:15]
	v_mfma_f32_16x16x32_f16 v[0:3], v[136:139], v[176:179], v[0:3]
	s_setprio 0
	s_barrier
	s_mov_b32 m0, s47
	ds_read_b128 v[132:135], v131 offset:57344
	ds_read_b128 v[136:139], v131 offset:58368
	ds_read_b128 v[140:143], v131 offset:59392
	ds_read_b128 v[144:147], v131 offset:60416
	ds_read_b128 v[148:151], v182 offset:40960
	ds_read_b128 v[152:155], v182 offset:41984
	ds_read_b128 v[156:159], v182 offset:43008
	ds_read_b128 v[160:163], v182 offset:44032
	ds_read_b128 v[164:167], v182 offset:45056
	ds_read_b128 v[168:171], v182 offset:46080
	ds_read_b128 v[172:175], v182 offset:47104
	ds_read_b128 v[176:179], v182 offset:48128
	global_load_lds_dwordx4 v48, s[66:67]
	s_mov_b32 m0, s48
	s_nop 0
	global_load_lds_dwordx4 v52, s[66:67]
	s_barrier
	s_setprio 1
	s_waitcnt lgkmcnt(7)
	v_mfma_f32_16x16x32_f16 v[40:43], v[132:135], v[148:151], v[40:43]
	v_mfma_f32_16x16x32_f16 v[44:47], v[140:143], v[148:151], v[44:47]
	s_waitcnt lgkmcnt(5)
	v_mfma_f32_16x16x32_f16 v[32:35], v[132:135], v[156:159], v[32:35]
	v_mfma_f32_16x16x32_f16 v[28:31], v[140:143], v[156:159], v[28:31]
	s_waitcnt lgkmcnt(3)
	v_mfma_f32_16x16x32_f16 v[20:23], v[132:135], v[164:167], v[20:23]
	v_mfma_f32_16x16x32_f16 v[16:19], v[140:143], v[164:167], v[16:19]
	s_waitcnt lgkmcnt(1)
	v_mfma_f32_16x16x32_f16 v[8:11], v[132:135], v[172:175], v[8:11]
	v_mfma_f32_16x16x32_f16 v[4:7], v[140:143], v[172:175], v[4:7]
	v_mfma_f32_16x16x32_f16 v[40:43], v[136:139], v[152:155], v[40:43]
	v_mfma_f32_16x16x32_f16 v[44:47], v[144:147], v[152:155], v[44:47]
	v_mfma_f32_16x16x32_f16 v[32:35], v[136:139], v[160:163], v[32:35]
	v_mfma_f32_16x16x32_f16 v[28:31], v[144:147], v[160:163], v[28:31]
	v_mfma_f32_16x16x32_f16 v[20:23], v[136:139], v[168:171], v[20:23]
	v_mfma_f32_16x16x32_f16 v[16:19], v[144:147], v[168:171], v[16:19]
	s_waitcnt lgkmcnt(0)
	v_mfma_f32_16x16x32_f16 v[8:11], v[136:139], v[176:179], v[8:11]
	v_mfma_f32_16x16x32_f16 v[4:7], v[144:147], v[176:179], v[4:7]
	s_setprio 0
	s_barrier
	s_mov_b32 m0, s49
	ds_read_b128 v[132:135], v131 offset:61440
	ds_read_b128 v[136:139], v131 offset:62464
	global_load_lds_dwordx4 v50, s[30:31]
	s_mov_b32 m0, s50
	s_nop 0
	global_load_lds_dwordx4 v54, s[30:31]
	s_mov_b32 m0, s51
	s_nop 0
	global_load_lds_dwordx4 v56, s[30:31]
	s_cmp_eq_u32 s65, 0
	s_cbranch_scc1 .Lm2_first_1
	s_waitcnt vmcnt(5)
.Lm2_join_1:
	s_barrier
	s_setprio 1
	s_waitcnt lgkmcnt(1)
	v_mfma_f32_16x16x32_f16 v[36:39], v[132:135], v[148:151], v[36:39]
	v_mfma_f32_16x16x32_f16 v[24:27], v[132:135], v[156:159], v[24:27]
	v_mfma_f32_16x16x32_f16 v[12:15], v[132:135], v[164:167], v[12:15]
	v_mfma_f32_16x16x32_f16 v[0:3], v[132:135], v[172:175], v[0:3]
	s_waitcnt lgkmcnt(0)
	v_mfma_f32_16x16x32_f16 v[36:39], v[136:139], v[152:155], v[36:39]
	v_mfma_f32_16x16x32_f16 v[24:27], v[136:139], v[160:163], v[24:27]
	v_mfma_f32_16x16x32_f16 v[12:15], v[136:139], v[168:171], v[12:15]
	v_mfma_f32_16x16x32_f16 v[0:3], v[136:139], v[176:179], v[0:3]
	s_setprio 0
	s_barrier
	s_mov_b32 m0, s54
	v_add_u32_e32 v131, s62, v127
	ds_read_b128 v[132:135], v130
	ds_read_b128 v[136:139], v130 offset:1024
	ds_read_b128 v[140:143], v130 offset:2048
	ds_read_b128 v[144:147], v130 offset:3072
	ds_read_b128 v[148:151], v131
	ds_read_b128 v[152:155], v131 offset:1024
	ds_read_b128 v[156:159], v131 offset:2048
	ds_read_b128 v[160:163], v131 offset:3072
	ds_read_b128 v[164:167], v131 offset:4096
	ds_read_b128 v[168:171], v131 offset:5120
	ds_read_b128 v[172:175], v131 offset:6144
	ds_read_b128 v[176:179], v131 offset:7168
	global_load_lds_dwordx4 v48, s[76:77]
	s_mov_b32 m0, s55
	s_nop 0
	global_load_lds_dwordx4 v52, s[76:77]
	s_barrier
	s_setprio 1
	s_waitcnt lgkmcnt(7)
	v_mfma_f32_16x16x32_f16 v[40:43], v[132:135], v[148:151], v[40:43]
	v_mfma_f32_16x16x32_f16 v[44:47], v[140:143], v[148:151], v[44:47]
	s_waitcnt lgkmcnt(5)
	v_mfma_f32_16x16x32_f16 v[32:35], v[132:135], v[156:159], v[32:35]
	v_mfma_f32_16x16x32_f16 v[28:31], v[140:143], v[156:159], v[28:31]
	s_waitcnt lgkmcnt(3)
	v_mfma_f32_16x16x32_f16 v[20:23], v[132:135], v[164:167], v[20:23]
	v_mfma_f32_16x16x32_f16 v[16:19], v[140:143], v[164:167], v[16:19]
	s_waitcnt lgkmcnt(1)
	v_mfma_f32_16x16x32_f16 v[8:11], v[132:135], v[172:175], v[8:11]
	v_mfma_f32_16x16x32_f16 v[4:7], v[140:143], v[172:175], v[4:7]
	v_mfma_f32_16x16x32_f16 v[40:43], v[136:139], v[152:155], v[40:43]
	v_mfma_f32_16x16x32_f16 v[44:47], v[144:147], v[152:155], v[44:47]
	v_mfma_f32_16x16x32_f16 v[32:35], v[136:139], v[160:163], v[32:35]
	v_mfma_f32_16x16x32_f16 v[28:31], v[144:147], v[160:163], v[28:31]
	v_mfma_f32_16x16x32_f16 v[20:23], v[136:139], v[168:171], v[20:23]
	v_mfma_f32_16x16x32_f16 v[16:19], v[144:147], v[168:171], v[16:19]
	s_waitcnt lgkmcnt(0)
	v_mfma_f32_16x16x32_f16 v[8:11], v[136:139], v[176:179], v[8:11]
	v_mfma_f32_16x16x32_f16 v[4:7], v[144:147], v[176:179], v[4:7]
	s_setprio 0
	s_barrier
	s_mov_b32 m0, s56
	ds_read_b128 v[132:135], v130 offset:4096
	ds_read_b128 v[136:139], v130 offset:5120
	global_load_lds_dwordx4 v50, s[78:79]
	s_add_i32 m0, s56, 0x2000
	s_nop 0
	global_load_lds_dwordx4 v54, s[78:79]
	s_add_i32 m0, s56, 0x4000
	s_nop 0
	global_load_lds_dwordx4 v56, s[78:79]
	s_cmp_eq_u32 s65, 0
	s_cbranch_scc1 .Lm2_first_2
	s_waitcnt vmcnt(5)

.Lm2_first_0:
	s_mul_i32 s70, s58, 0xc0
	v_add_u32_e32 v234, s70, v129
	v_ashrrev_i32_e32 v235, 31, v234
	v_lshlrev_b64 v[234:235], 2, v[234:235]
	v_lshl_add_u64 v[234:235], s[18:19], 0, v[234:235]
	global_load_dwordx4 v[222:225], v[234:235], off
	global_load_dwordx4 v[226:229], v[234:235], off offset:64
	global_load_dwordx4 v[230:233], v[234:235], off offset:128
	global_load_dwordx2 v[198:199], v[190:191], off
	global_load_dwordx2 v[200:201], v[190:191], off offset:32
	global_load_dwordx2 v[202:203], v[190:191], off offset:64
	global_load_dwordx2 v[204:205], v[192:193], off
	s_waitcnt vmcnt(12)
	s_branch .Lm2_join_0
.Lm2_first_1:
	global_load_dwordx2 v[206:207], v[192:193], off offset:32
	global_load_dwordx2 v[208:209], v[192:193], off offset:64
	global_load_dwordx2 v[210:211], v[194:195], off
	global_load_dwordx2 v[212:213], v[194:195], off offset:32
	s_waitcnt vmcnt(16)
	s_branch .Lm2_join_1
.Lm2_first_2:
	global_load_dwordx2 v[214:215], v[194:195], off offset:64
	global_load_dwordx2 v[216:217], v[196:197], off
	global_load_dwordx2 v[218:219], v[196:197], off offset:32
	global_load_dwordx2 v[220:221], v[196:197], off offset:64
	s_waitcnt vmcnt(13)
	s_branch .Lm2_join_2
